# speedup vs baseline: 1.0085x; 1.0085x over previous
.LBB1_108:
	s_load_dwordx2 s[24:25], s[0:1], 0x38
	s_cmp_eq_u32 s3, 1
	s_cselect_b32 s6, s16, s14
	s_cselect_b32 s7, s17, s15
	s_lshr_b32 s23, s22, 3
	s_and_b32 s26, s21, 0x700
	s_waitcnt lgkmcnt(0)
	s_barrier
	s_cmp_lt_u32 s2, 64
	s_cbranch_scc1 .Lqkv_out_v
	s_mov_b32 s27, 0xaaaaaab
	v_mul_hi_u32 v1, v0, s27
	v_mul_u32_u24_e32 v2, 24, v1
	v_sub_u32_e32 v2, v0, v2
	v_lshl_add_u32 v3, v2, 3, s20
	v_mul_u32_u24_e32 v5, 0x190, v1
	v_lshl_add_u32 v5, v2, 4, v5
	v_add_u32_e32 v6, 0xc800, v5
	ds_read_b128 v[16:19], v5
	ds_read_b128 v[20:23], v5 offset:12800
	ds_read_b128 v[24:27], v5 offset:25600
	ds_read_b128 v[28:31], v5 offset:38400
	ds_read_b128 v[32:35], v6
	ds_read_b128 v[36:39], v6 offset:12800
	ds_read_b128 v[40:43], v6 offset:25600
	ds_read_b128 v[44:47], v6 offset:38400
	v_lshrrev_b32_e32 v7, 6, v3
	s_mul_i32 s27, s23, 12
	v_add_u32_e32 v7, s27, v7
	v_lshlrev_b32_e32 v7, 18, v7
	v_and_b32_e32 v48, 63, v3
	v_lshlrev_b32_e32 v48, 1, v48
	v_add_u32_e32 v49, s26, v1
	v_lshl_add_u32 v48, v49, 7, v48
	v_add_u32_e32 v7, v7, v48
	s_waitcnt lgkmcnt(7)
	global_store_dwordx4 v7, v[16:19], s[6:7] sc0 sc1
	v_add_u32_e32 v7, 0x1000, v7
	s_waitcnt lgkmcnt(6)
	global_store_dwordx4 v7, v[20:23], s[6:7] sc0 sc1
	v_add_u32_e32 v7, 0x1000, v7
	s_waitcnt lgkmcnt(5)
	global_store_dwordx4 v7, v[24:27], s[6:7] sc0 sc1
	v_add_u32_e32 v7, 0x1000, v7
	s_waitcnt lgkmcnt(4)
	global_store_dwordx4 v7, v[28:31], s[6:7] sc0 sc1
	v_add_u32_e32 v7, 0x1000, v7
	s_waitcnt lgkmcnt(3)
	global_store_dwordx4 v7, v[32:35], s[6:7] sc0 sc1
	v_add_u32_e32 v7, 0x1000, v7
	s_waitcnt lgkmcnt(2)
	global_store_dwordx4 v7, v[36:39], s[6:7] sc0 sc1
	v_add_u32_e32 v7, 0x1000, v7
	s_waitcnt lgkmcnt(1)
	global_store_dwordx4 v7, v[40:43], s[6:7] sc0 sc1
	v_add_u32_e32 v7, 0x1000, v7
	s_waitcnt lgkmcnt(0)
	global_store_dwordx4 v7, v[44:47], s[6:7] sc0 sc1
	s_endpgm
.Lqkv_out_v:
	v_lshrrev_b32_e32 v1, 5, v0
	v_and_b32_e32 v2, 31, v0
	v_add_u32_e32 v3, s20, v1
	v_mul_u32_u24_e32 v5, 0x210, v1
	v_lshl_add_u32 v5, v2, 4, v5
	v_add_u32_e32 v6, 0xc600, v5
	ds_read_b128 v[16:19], v5
	ds_read_b128 v[20:23], v5 offset:12672
	ds_read_b128 v[24:27], v5 offset:25344
	ds_read_b128 v[28:31], v5 offset:38016
	ds_read_b128 v[32:35], v6
	ds_read_b128 v[36:39], v6 offset:12672
	ds_read_b128 v[40:43], v6 offset:25344
	ds_read_b128 v[44:47], v6 offset:38016
	s_mul_i32 s27, s23, 0x300
	v_add_u32_e32 v7, s27, v3
	v_lshlrev_b32_e32 v7, 12, v7
	v_lshl_add_u32 v48, v2, 3, s26
	v_lshl_add_u32 v7, v48, 1, v7
	s_waitcnt lgkmcnt(7)
	global_store_dwordx4 v7, v[16:19], s[24:25] sc0 sc1
	v_add_u32_e32 v7, 0x18000, v7
	s_waitcnt lgkmcnt(6)
	global_store_dwordx4 v7, v[20:23], s[24:25] sc0 sc1
	v_add_u32_e32 v7, 0x18000, v7
	s_waitcnt lgkmcnt(5)
	global_store_dwordx4 v7, v[24:27], s[24:25] sc0 sc1
	v_add_u32_e32 v7, 0x18000, v7
	s_waitcnt lgkmcnt(4)
	global_store_dwordx4 v7, v[28:31], s[24:25] sc0 sc1
	v_add_u32_e32 v7, 0x18000, v7
	s_waitcnt lgkmcnt(3)
	global_store_dwordx4 v7, v[32:35], s[24:25] sc0 sc1
	v_add_u32_e32 v7, 0x18000, v7
	s_waitcnt lgkmcnt(2)
	global_store_dwordx4 v7, v[36:39], s[24:25] sc0 sc1
	v_add_u32_e32 v7, 0x18000, v7
	s_waitcnt lgkmcnt(1)
	global_store_dwordx4 v7, v[40:43], s[24:25] sc0 sc1
	v_add_u32_e32 v7, 0x18000, v7
	s_waitcnt lgkmcnt(0)
	global_store_dwordx4 v7, v[44:47], s[24:25] sc0 sc1
	s_endpgm
